# speedup vs baseline: 1.0161x; 1.0011x over previous
_Z13stage0_kernel5TJobs6S0Args:
	s_mov_b32 s3, 0xa1e
	s_cmpk_lt_u32 s2, 0x409
	s_cselect_b32 s3, s3, 0xfffffbf7
	s_add_i32 s2, s2, s3
	s_load_dwordx16 s[4:19], s[0:1], 0x120
	s_load_dwordx16 s[36:51], s[0:1], 0x1e0
	s_add_u32 s34, s0, 0x120
	s_addc_u32 s35, s1, 0
	s_cmpk_gt_i32 s2, 0xcb
	s_waitcnt lgkmcnt(0)
	v_writelane_b32 v83, s4, 0
	s_nop 1
	v_writelane_b32 v83, s5, 1
	v_writelane_b32 v83, s6, 2
	v_writelane_b32 v83, s7, 3
	v_writelane_b32 v83, s8, 4
	v_writelane_b32 v83, s9, 5
	v_writelane_b32 v83, s10, 6
	v_writelane_b32 v83, s11, 7
	v_writelane_b32 v83, s12, 8
	v_writelane_b32 v83, s13, 9
	v_writelane_b32 v83, s14, 10
	v_writelane_b32 v83, s15, 11
	v_writelane_b32 v83, s16, 12
	v_writelane_b32 v83, s17, 13
	v_writelane_b32 v83, s18, 14
	v_writelane_b32 v83, s19, 15
	s_mov_b64 s[4:5], -1
	s_cbranch_scc0 .LBB0_116
	s_load_dword s4, s[34:35], 0x114
	s_add_i32 s3, s2, 0xffffff34
	v_writelane_b32 v83, s3, 16
	s_waitcnt lgkmcnt(0)
	s_cmp_ge_i32 s3, s4
	s_mov_b32 s3, s4
	s_mov_b64 s[4:5], -1
	s_cbranch_scc0 .LBB0_93
	s_mov_b32 s4, s3
	s_load_dword s3, s[0:1], 0x230
	s_waitcnt lgkmcnt(0)
	s_add_i32 s3, s3, s4
	v_readlane_b32 s4, v83, 16
	s_cmp_ge_i32 s4, s3
	s_mov_b64 s[4:5], -1
	s_cbranch_scc0 .LBB0_80
	s_sub_i32 s4, s2, 0xcc
	s_sub_i32 s4, s4, s3
	s_load_dwordx2 s[8:9], s[0:1], 0x198
	s_load_dwordx16 s[12:27], s[0:1], 0x1a0
	s_load_dwordx4 s[28:31], s[0:1], 0x1e0
	v_lshlrev_b32_e32 v5, 5, v0
	v_and_b32_e32 v6, 0x7f, v0
	v_lshlrev_b32_e32 v6, 4, v6
	s_waitcnt lgkmcnt(0)
	global_load_dwordx4 v[8:11], v5, s[16:17]
	global_load_dwordx4 v[12:15], v5, s[16:17] offset:16
	global_load_dwordx4 v[16:19], v6, s[26:27]
	s_waitcnt vmcnt(0)
	ds_write_b128 v5, v[8:11]
	ds_write_b128 v5, v[12:15] offset:16
	ds_write_b128 v6, v[16:19] offset:8192
	s_waitcnt lgkmcnt(0)
	s_barrier
	v_lshrrev_b32_e32 v1, 7, v0
	s_nop 0
	v_readfirstlane_b32 s33, v1
	v_and_b32_e32 v1, 0x7f, v0
	v_lshl_or_b32 v1, s4, 7, v1
	s_mov_b32 s5, 0x20460
	v_cmp_gt_u32_e32 vcc, s5, v1
	s_mov_b64 s[6:7], vcc
	v_min_u32_e32 v1, 0x2045f, v1
	v_mul_u32_u24_e32 v5, 12, v1
	v_and_b32_e32 v6, 63, v0
	v_lshlrev_b32_e32 v6, 2, v6
	v_and_b32_e32 v7, 15, v0
	v_lshlrev_b32_e32 v7, 2, v7
	s_mov_b32 s5, 0xf0f0f0f1
	v_mul_hi_u32 v77, v1, s5
	v_lshrrev_b32_e32 v77, 4, v77
	v_lshl_add_u32 v77, v77, 4, v77
	v_sub_u32_e32 v77, v1, v77
	v_lshlrev_b32_e32 v77, 7, v77
	s_waitcnt lgkmcnt(0)
	global_load_dwordx3 v[2:4], v5, s[8:9]
	global_load_dword v72, v6, s[12:13]
	global_load_dword v73, v6, s[12:13] offset:256
	global_load_dword v74, v6, s[14:15]
	global_load_dword v75, v7, s[22:23]
	global_load_dword v76, v7, s[24:25]
	v_mov_b32_e32 v6, v77
	v_and_b32_e32 v5, 0x7f, v0
	v_lshlrev_b32_e32 v5, 2, v5
	v_add_u32_e32 v5, 0x2800, v5
	v_mul_u32_u24_e32 v1, 0x480, v1
	v_mov_b32_e32 v84, 0x378e98ab
	v_mov_b32_e32 v85, 0xb9c68948
	v_mov_b32_e32 v86, 0x3b7cd369
	v_mov_b32_e32 v87, 0xbcc618b2
	v_mov_b32_e32 v88, 0x3dda74e4
	v_mov_b32_e32 v89, 0x3f228afd
	v_mov_b32_e32 v90, 0x3ba10414
	v_mov_b32_e32 v91, 0x3e03c728
	v_mov_b32_e32 v92, 0xbfb8aa3b
	v_mov_b32_e32 v93, 0x42ce8ed0
	v_mov_b32_e32 v94, 0xc2b17218
	v_mov_b32_e32 v95, 0x7f800000
	s_brev_b32 s0, -2
	s_cmp_eq_u32 s33, 0
	s_cbranch_scc0 .Lfeat_zc
	s_load_dwordx16 s[36:51], s[18:19], 0x0
	s_load_dwordx16 s[52:67], s[18:19], 0x40
	s_waitcnt lgkmcnt(0)
	v_mov_b32_e32 v8, s36
	v_mov_b32_e32 v9, s37
	v_mov_b32_e32 v10, s38
	v_mov_b32_e32 v11, s39
	v_mov_b32_e32 v12, s40
	v_mov_b32_e32 v13, s41
	v_mov_b32_e32 v14, s42
	v_mov_b32_e32 v15, s43
	v_mov_b32_e32 v16, s44
	v_mov_b32_e32 v17, s45
	v_mov_b32_e32 v18, s46
	v_mov_b32_e32 v19, s47
	v_mov_b32_e32 v20, s48
	v_mov_b32_e32 v21, s49
	v_mov_b32_e32 v22, s50
	v_mov_b32_e32 v23, s51
	v_mov_b32_e32 v24, s52
	v_mov_b32_e32 v25, s53
	v_mov_b32_e32 v26, s54
	v_mov_b32_e32 v27, s55
	v_mov_b32_e32 v28, s56
	v_mov_b32_e32 v29, s57
	v_mov_b32_e32 v30, s58
	v_mov_b32_e32 v31, s59
	v_mov_b32_e32 v32, s60
	v_mov_b32_e32 v33, s61
	v_mov_b32_e32 v34, s62
	v_mov_b32_e32 v35, s63
	v_mov_b32_e32 v36, s64
	v_mov_b32_e32 v37, s65
	v_mov_b32_e32 v38, s66
	v_mov_b32_e32 v39, s67
	s_branch .Lfeat_gc
.Lfeat_zc:
	v_mov_b32_e32 v8, 0
	v_mov_b32_e32 v9, 0
	v_mov_b32_e32 v10, 0
	v_mov_b32_e32 v11, 0
	v_mov_b32_e32 v12, 0
	v_mov_b32_e32 v13, 0
	v_mov_b32_e32 v14, 0
	v_mov_b32_e32 v15, 0
	v_mov_b32_e32 v16, 0
	v_mov_b32_e32 v17, 0
	v_mov_b32_e32 v18, 0
	v_mov_b32_e32 v19, 0
	v_mov_b32_e32 v20, 0
	v_mov_b32_e32 v21, 0
	v_mov_b32_e32 v22, 0
	v_mov_b32_e32 v23, 0
	v_mov_b32_e32 v24, 0
	v_mov_b32_e32 v25, 0
	v_mov_b32_e32 v26, 0
	v_mov_b32_e32 v27, 0
	v_mov_b32_e32 v28, 0
	v_mov_b32_e32 v29, 0
	v_mov_b32_e32 v30, 0
	v_mov_b32_e32 v31, 0
	v_mov_b32_e32 v32, 0
	v_mov_b32_e32 v33, 0
	v_mov_b32_e32 v34, 0
	v_mov_b32_e32 v35, 0
	v_mov_b32_e32 v36, 0
	v_mov_b32_e32 v37, 0
	v_mov_b32_e32 v38, 0
	v_mov_b32_e32 v39, 0
.Lfeat_gc:
	s_waitcnt vmcnt(0)
	s_lshl_b32 s10, s33, 5
	s_add_u32 s34, s10, 32
	s_lshl_b32 s1, s10, 7
	s_add_u32 s1, s1, 0x0
	v_mov_b32_e32 v7, s1

.Lfeat_nl_c1:
	s_mov_b64 exec, s[8:9]
	v_bfi_b32 v81, s0, v81, v78
	v_mul_f32_e32 v80, 0.5, v77
	v_add_f32_e32 v81, 1.0, v81
	v_mul_f32_e32 v80, v80, v81
	s_waitcnt lgkmcnt(0)
	v_fmac_f32_e32 v8, v40, v80
	v_fmac_f32_e32 v9, v41, v80
	v_fmac_f32_e32 v10, v42, v80
	v_fmac_f32_e32 v11, v43, v80
	v_fmac_f32_e32 v12, v44, v80
	v_fmac_f32_e32 v13, v45, v80
	v_fmac_f32_e32 v14, v46, v80
	v_fmac_f32_e32 v15, v47, v80
	v_fmac_f32_e32 v16, v48, v80
	v_fmac_f32_e32 v17, v49, v80
	v_fmac_f32_e32 v18, v50, v80
	v_fmac_f32_e32 v19, v51, v80
	v_fmac_f32_e32 v20, v52, v80
	v_fmac_f32_e32 v21, v53, v80
	v_fmac_f32_e32 v22, v54, v80
	v_fmac_f32_e32 v23, v55, v80
	v_fmac_f32_e32 v24, v56, v80
	v_fmac_f32_e32 v25, v57, v80
	v_fmac_f32_e32 v26, v58, v80
	v_fmac_f32_e32 v27, v59, v80
	v_fmac_f32_e32 v28, v60, v80
	v_fmac_f32_e32 v29, v61, v80
	v_fmac_f32_e32 v30, v62, v80
	v_fmac_f32_e32 v31, v63, v80
	v_fmac_f32_e32 v32, v64, v80
	v_fmac_f32_e32 v33, v65, v80
	v_fmac_f32_e32 v34, v66, v80
	v_fmac_f32_e32 v35, v67, v80
	v_fmac_f32_e32 v36, v68, v80
	v_fmac_f32_e32 v37, v69, v80
	v_fmac_f32_e32 v38, v70, v80
	v_fmac_f32_e32 v39, v71, v80
	s_add_u32 s10, s10, 2
	s_cmp_lt_u32 s10, s34
	s_cbranch_scc1 .Lfeat_loop_c
	s_cmp_eq_u32 s33, 0
	s_cbranch_scc1 .Lfeat_c_nw
	ds_write_b32 v5, v8 offset:0
	ds_write_b32 v5, v9 offset:512
	ds_write_b32 v5, v10 offset:1024
	ds_write_b32 v5, v11 offset:1536
	ds_write_b32 v5, v12 offset:2048
	ds_write_b32 v5, v13 offset:2560
	ds_write_b32 v5, v14 offset:3072
	ds_write_b32 v5, v15 offset:3584
	ds_write_b32 v5, v16 offset:4096
	ds_write_b32 v5, v17 offset:4608
	ds_write_b32 v5, v18 offset:5120
	ds_write_b32 v5, v19 offset:5632
	ds_write_b32 v5, v20 offset:6144
	ds_write_b32 v5, v21 offset:6656
	ds_write_b32 v5, v22 offset:7168
	ds_write_b32 v5, v23 offset:7680
	ds_write_b32 v5, v24 offset:8192
	ds_write_b32 v5, v25 offset:8704
	ds_write_b32 v5, v26 offset:9216
	ds_write_b32 v5, v27 offset:9728
	ds_write_b32 v5, v28 offset:10240
	ds_write_b32 v5, v29 offset:10752
	ds_write_b32 v5, v30 offset:11264
	ds_write_b32 v5, v31 offset:11776
	ds_write_b32 v5, v32 offset:12288
	ds_write_b32 v5, v33 offset:12800
	ds_write_b32 v5, v34 offset:13312
	ds_write_b32 v5, v35 offset:13824
	ds_write_b32 v5, v36 offset:14336
	ds_write_b32 v5, v37 offset:14848
	ds_write_b32 v5, v38 offset:15360
	ds_write_b32 v5, v39 offset:15872
	s_waitcnt lgkmcnt(0)
.Lfeat_c_nw:
	s_barrier
	s_cmp_eq_u32 s33, 0
	s_cbranch_scc0 .Lfeat_c_nf
	ds_read_b32 v40, v5 offset:0
	ds_read_b32 v41, v5 offset:512
	ds_read_b32 v42, v5 offset:1024
	ds_read_b32 v43, v5 offset:1536
	ds_read_b32 v44, v5 offset:2048
	ds_read_b32 v45, v5 offset:2560
	ds_read_b32 v46, v5 offset:3072
	ds_read_b32 v47, v5 offset:3584
	ds_read_b32 v48, v5 offset:4096
	ds_read_b32 v49, v5 offset:4608
	ds_read_b32 v50, v5 offset:5120
	ds_read_b32 v51, v5 offset:5632
	ds_read_b32 v52, v5 offset:6144
	ds_read_b32 v53, v5 offset:6656
	ds_read_b32 v54, v5 offset:7168
	ds_read_b32 v55, v5 offset:7680
	ds_read_b32 v56, v5 offset:8192
	ds_read_b32 v57, v5 offset:8704
	ds_read_b32 v58, v5 offset:9216
	ds_read_b32 v59, v5 offset:9728
	ds_read_b32 v60, v5 offset:10240
	ds_read_b32 v61, v5 offset:10752
	ds_read_b32 v62, v5 offset:11264
	ds_read_b32 v63, v5 offset:11776
	ds_read_b32 v64, v5 offset:12288
	ds_read_b32 v65, v5 offset:12800
	ds_read_b32 v66, v5 offset:13312
	ds_read_b32 v67, v5 offset:13824
	ds_read_b32 v68, v5 offset:14336
	ds_read_b32 v69, v5 offset:14848
	ds_read_b32 v70, v5 offset:15360
	ds_read_b32 v71, v5 offset:15872
	s_waitcnt lgkmcnt(0)
	v_add_f32_e32 v8, v8, v40
	v_add_f32_e32 v9, v9, v41
	v_add_f32_e32 v10, v10, v42
	v_add_f32_e32 v11, v11, v43
	v_add_f32_e32 v12, v12, v44
	v_add_f32_e32 v13, v13, v45
	v_add_f32_e32 v14, v14, v46
	v_add_f32_e32 v15, v15, v47
	v_add_f32_e32 v16, v16, v48
	v_add_f32_e32 v17, v17, v49
	v_add_f32_e32 v18, v18, v50
	v_add_f32_e32 v19, v19, v51
	v_add_f32_e32 v20, v20, v52
	v_add_f32_e32 v21, v21, v53
	v_add_f32_e32 v22, v22, v54
	v_add_f32_e32 v23, v23, v55
	v_add_f32_e32 v24, v24, v56
	v_add_f32_e32 v25, v25, v57
	v_add_f32_e32 v26, v26, v58
	v_add_f32_e32 v27, v27, v59
	v_add_f32_e32 v28, v28, v60
	v_add_f32_e32 v29, v29, v61
	v_add_f32_e32 v30, v30, v62
	v_add_f32_e32 v31, v31, v63
	v_add_f32_e32 v32, v32, v64
	v_add_f32_e32 v33, v33, v65
	v_add_f32_e32 v34, v34, v66
	v_add_f32_e32 v35, v35, v67
	v_add_f32_e32 v36, v36, v68
	v_add_f32_e32 v37, v37, v69
	v_add_f32_e32 v38, v38, v70
	v_add_f32_e32 v39, v39, v71
	global_load_dwordx4 v[40:43], v6, s[20:21] offset:0
	global_load_dwordx4 v[44:47], v6, s[20:21] offset:16
	global_load_dwordx4 v[48:51], v6, s[20:21] offset:32
	global_load_dwordx4 v[52:55], v6, s[20:21] offset:48
	global_load_dwordx4 v[56:59], v6, s[20:21] offset:64
	global_load_dwordx4 v[60:63], v6, s[20:21] offset:80
	global_load_dwordx4 v[64:67], v6, s[20:21] offset:96
	global_load_dwordx4 v[68:71], v6, s[20:21] offset:112
	s_waitcnt vmcnt(0)
	v_cmp_lt_f32_e32 vcc, 0.5, v4
	v_add_f32_e32 v8, v8, v40
	v_add_f32_e32 v9, v9, v41
	v_add_f32_e32 v10, v10, v42
	v_add_f32_e32 v11, v11, v43
	v_add_f32_e32 v12, v12, v44
	v_add_f32_e32 v13, v13, v45
	v_add_f32_e32 v14, v14, v46
	v_add_f32_e32 v15, v15, v47
	v_add_f32_e32 v16, v16, v48
	v_add_f32_e32 v17, v17, v49
	v_add_f32_e32 v18, v18, v50
	v_add_f32_e32 v19, v19, v51
	v_add_f32_e32 v20, v20, v52
	v_add_f32_e32 v21, v21, v53
	v_add_f32_e32 v22, v22, v54
	v_add_f32_e32 v23, v23, v55
	v_add_f32_e32 v24, v24, v56
	v_add_f32_e32 v25, v25, v57
	v_add_f32_e32 v26, v26, v58
	v_add_f32_e32 v27, v27, v59
	v_add_f32_e32 v28, v28, v60
	v_add_f32_e32 v29, v29, v61
	v_add_f32_e32 v30, v30, v62
	v_add_f32_e32 v31, v31, v63
	v_add_f32_e32 v32, v32, v64
	v_add_f32_e32 v33, v33, v65
	v_add_f32_e32 v34, v34, v66
	v_add_f32_e32 v35, v35, v67
	v_add_f32_e32 v36, v36, v68
	v_add_f32_e32 v37, v37, v69
	v_add_f32_e32 v38, v38, v70
	v_add_f32_e32 v39, v39, v71
	v_cndmask_b32_e32 v8, v40, v8, vcc
	v_cndmask_b32_e32 v9, v41, v9, vcc
	v_cndmask_b32_e32 v10, v42, v10, vcc
	v_cndmask_b32_e32 v11, v43, v11, vcc
	v_cndmask_b32_e32 v12, v44, v12, vcc
	v_cndmask_b32_e32 v13, v45, v13, vcc
	v_cndmask_b32_e32 v14, v46, v14, vcc
	v_cndmask_b32_e32 v15, v47, v15, vcc
	v_cndmask_b32_e32 v16, v48, v16, vcc
	v_cndmask_b32_e32 v17, v49, v17, vcc
	v_cndmask_b32_e32 v18, v50, v18, vcc
	v_cndmask_b32_e32 v19, v51, v19, vcc
	v_cndmask_b32_e32 v20, v52, v20, vcc
	v_cndmask_b32_e32 v21, v53, v21, vcc
	v_cndmask_b32_e32 v22, v54, v22, vcc
	v_cndmask_b32_e32 v23, v55, v23, vcc
	v_cndmask_b32_e32 v24, v56, v24, vcc
	v_cndmask_b32_e32 v25, v57, v25, vcc
	v_cndmask_b32_e32 v26, v58, v26, vcc
	v_cndmask_b32_e32 v27, v59, v27, vcc
	v_cndmask_b32_e32 v28, v60, v28, vcc
	v_cndmask_b32_e32 v29, v61, v29, vcc
	v_cndmask_b32_e32 v30, v62, v30, vcc
	v_cndmask_b32_e32 v31, v63, v31, vcc
	v_cndmask_b32_e32 v32, v64, v32, vcc
	v_cndmask_b32_e32 v33, v65, v33, vcc
	v_cndmask_b32_e32 v34, v66, v34, vcc
	v_cndmask_b32_e32 v35, v67, v35, vcc
	v_cndmask_b32_e32 v36, v68, v36, vcc
	v_cndmask_b32_e32 v37, v69, v37, vcc
	v_cndmask_b32_e32 v38, v70, v38, vcc
	v_cndmask_b32_e32 v39, v71, v39, vcc
	s_mov_b64 s[8:9], exec
	s_and_b64 exec, exec, s[6:7]
	v_cvt_pk_f16_f32 v80, v8, v9
	v_cvt_pk_f16_f32 v81, v10, v11
	v_cvt_pk_f16_f32 v82, v12, v13
	v_cvt_pk_f16_f32 v83, v14, v15
	global_store_dwordx4 v1, v[80:83], s[30:31] offset:1024
	s_nop 1
	v_cvt_pk_f16_f32 v80, v16, v17
	v_cvt_pk_f16_f32 v81, v18, v19
	v_cvt_pk_f16_f32 v82, v20, v21
	v_cvt_pk_f16_f32 v83, v22, v23
	global_store_dwordx4 v1, v[80:83], s[30:31] offset:1040
	s_nop 1
	v_cvt_pk_f16_f32 v80, v24, v25
	v_cvt_pk_f16_f32 v81, v26, v27
	v_cvt_pk_f16_f32 v82, v28, v29
	v_cvt_pk_f16_f32 v83, v30, v31
	global_store_dwordx4 v1, v[80:83], s[30:31] offset:1056
	s_nop 1
	v_cvt_pk_f16_f32 v80, v32, v33
	v_cvt_pk_f16_f32 v81, v34, v35
	v_cvt_pk_f16_f32 v82, v36, v37
	v_cvt_pk_f16_f32 v83, v38, v39
	global_store_dwordx4 v1, v[80:83], s[30:31] offset:1072
	s_mov_b64 exec, s[8:9]
	s_nop 1
.Lfeat_c_nf:
	s_cmp_eq_u32 s33, 0
	s_cbranch_scc0 .Lfeat_zf
	s_load_dwordx16 s[36:51], s[28:29], 0x0
	s_load_dwordx16 s[52:67], s[28:29], 0x40
	s_waitcnt lgkmcnt(0)
	v_mov_b32_e32 v8, s36
	v_mov_b32_e32 v9, s37
	v_mov_b32_e32 v10, s38
	v_mov_b32_e32 v11, s39
	v_mov_b32_e32 v12, s40
	v_mov_b32_e32 v13, s41
	v_mov_b32_e32 v14, s42
	v_mov_b32_e32 v15, s43
	v_mov_b32_e32 v16, s44
	v_mov_b32_e32 v17, s45
	v_mov_b32_e32 v18, s46
	v_mov_b32_e32 v19, s47
	v_mov_b32_e32 v20, s48
	v_mov_b32_e32 v21, s49
	v_mov_b32_e32 v22, s50
	v_mov_b32_e32 v23, s51
	v_mov_b32_e32 v24, s52
	v_mov_b32_e32 v25, s53
	v_mov_b32_e32 v26, s54
	v_mov_b32_e32 v27, s55
	v_mov_b32_e32 v28, s56
	v_mov_b32_e32 v29, s57
	v_mov_b32_e32 v30, s58
	v_mov_b32_e32 v31, s59
	v_mov_b32_e32 v32, s60
	v_mov_b32_e32 v33, s61
	v_mov_b32_e32 v34, s62
	v_mov_b32_e32 v35, s63
	v_mov_b32_e32 v36, s64
	v_mov_b32_e32 v37, s65
	v_mov_b32_e32 v38, s66
	v_mov_b32_e32 v39, s67
	s_branch .Lfeat_gf

.Lfeat_gf:
	s_lshl_b32 s10, s33, 3
	s_add_u32 s34, s10, 8
	s_lshl_b32 s1, s10, 7
	s_add_u32 s1, s1, 0x2000
	v_mov_b32_e32 v7, s1

.Lfeat_nl_f1:
	s_mov_b64 exec, s[8:9]
	v_bfi_b32 v81, s0, v81, v78
	v_mul_f32_e32 v80, 0.5, v77
	v_add_f32_e32 v81, 1.0, v81
	v_mul_f32_e32 v80, v80, v81
	s_waitcnt lgkmcnt(0)
	v_fmac_f32_e32 v8, v40, v80
	v_fmac_f32_e32 v9, v41, v80
	v_fmac_f32_e32 v10, v42, v80
	v_fmac_f32_e32 v11, v43, v80
	v_fmac_f32_e32 v12, v44, v80
	v_fmac_f32_e32 v13, v45, v80
	v_fmac_f32_e32 v14, v46, v80
	v_fmac_f32_e32 v15, v47, v80
	v_fmac_f32_e32 v16, v48, v80
	v_fmac_f32_e32 v17, v49, v80
	v_fmac_f32_e32 v18, v50, v80
	v_fmac_f32_e32 v19, v51, v80
	v_fmac_f32_e32 v20, v52, v80
	v_fmac_f32_e32 v21, v53, v80
	v_fmac_f32_e32 v22, v54, v80
	v_fmac_f32_e32 v23, v55, v80
	v_fmac_f32_e32 v24, v56, v80
	v_fmac_f32_e32 v25, v57, v80
	v_fmac_f32_e32 v26, v58, v80
	v_fmac_f32_e32 v27, v59, v80
	v_fmac_f32_e32 v28, v60, v80
	v_fmac_f32_e32 v29, v61, v80
	v_fmac_f32_e32 v30, v62, v80
	v_fmac_f32_e32 v31, v63, v80
	v_fmac_f32_e32 v32, v64, v80
	v_fmac_f32_e32 v33, v65, v80
	v_fmac_f32_e32 v34, v66, v80
	v_fmac_f32_e32 v35, v67, v80
	v_fmac_f32_e32 v36, v68, v80
	v_fmac_f32_e32 v37, v69, v80
	v_fmac_f32_e32 v38, v70, v80
	v_fmac_f32_e32 v39, v71, v80
	s_add_u32 s10, s10, 2
	s_cmp_lt_u32 s10, s34
	s_cbranch_scc1 .Lfeat_loop_f
	s_cmp_eq_u32 s33, 0
	s_cbranch_scc0 .Lfeat_f_nw
	ds_write_b32 v5, v8 offset:0
	ds_write_b32 v5, v9 offset:512
	ds_write_b32 v5, v10 offset:1024
	ds_write_b32 v5, v11 offset:1536
	ds_write_b32 v5, v12 offset:2048
	ds_write_b32 v5, v13 offset:2560
	ds_write_b32 v5, v14 offset:3072
	ds_write_b32 v5, v15 offset:3584
	ds_write_b32 v5, v16 offset:4096
	ds_write_b32 v5, v17 offset:4608
	ds_write_b32 v5, v18 offset:5120
	ds_write_b32 v5, v19 offset:5632
	ds_write_b32 v5, v20 offset:6144
	ds_write_b32 v5, v21 offset:6656
	ds_write_b32 v5, v22 offset:7168
	ds_write_b32 v5, v23 offset:7680
	ds_write_b32 v5, v24 offset:8192
	ds_write_b32 v5, v25 offset:8704
	ds_write_b32 v5, v26 offset:9216
	ds_write_b32 v5, v27 offset:9728
	ds_write_b32 v5, v28 offset:10240
	ds_write_b32 v5, v29 offset:10752
	ds_write_b32 v5, v30 offset:11264
	ds_write_b32 v5, v31 offset:11776
	ds_write_b32 v5, v32 offset:12288
	ds_write_b32 v5, v33 offset:12800
	ds_write_b32 v5, v34 offset:13312
	ds_write_b32 v5, v35 offset:13824
	ds_write_b32 v5, v36 offset:14336
	ds_write_b32 v5, v37 offset:14848
	ds_write_b32 v5, v38 offset:15360
	ds_write_b32 v5, v39 offset:15872
	s_waitcnt lgkmcnt(0)
.Lfeat_f_nw:
	s_barrier
	s_cmp_eq_u32 s33, 0
	s_cbranch_scc1 .Lfeat_done
	ds_read_b32 v40, v5 offset:0
	ds_read_b32 v41, v5 offset:512
	ds_read_b32 v42, v5 offset:1024
	ds_read_b32 v43, v5 offset:1536
	ds_read_b32 v44, v5 offset:2048
	ds_read_b32 v45, v5 offset:2560
	ds_read_b32 v46, v5 offset:3072
	ds_read_b32 v47, v5 offset:3584
	ds_read_b32 v48, v5 offset:4096
	ds_read_b32 v49, v5 offset:4608
	ds_read_b32 v50, v5 offset:5120
	ds_read_b32 v51, v5 offset:5632
	ds_read_b32 v52, v5 offset:6144
	ds_read_b32 v53, v5 offset:6656
	ds_read_b32 v54, v5 offset:7168
	ds_read_b32 v55, v5 offset:7680
	ds_read_b32 v56, v5 offset:8192
	ds_read_b32 v57, v5 offset:8704
	ds_read_b32 v58, v5 offset:9216
	ds_read_b32 v59, v5 offset:9728
	ds_read_b32 v60, v5 offset:10240
	ds_read_b32 v61, v5 offset:10752
	ds_read_b32 v62, v5 offset:11264
	ds_read_b32 v63, v5 offset:11776
	ds_read_b32 v64, v5 offset:12288
	ds_read_b32 v65, v5 offset:12800
	ds_read_b32 v66, v5 offset:13312
	ds_read_b32 v67, v5 offset:13824
	ds_read_b32 v68, v5 offset:14336
	ds_read_b32 v69, v5 offset:14848
	ds_read_b32 v70, v5 offset:15360
	ds_read_b32 v71, v5 offset:15872
	s_waitcnt lgkmcnt(0)
	v_add_f32_e32 v8, v8, v40
	v_add_f32_e32 v9, v9, v41
	v_add_f32_e32 v10, v10, v42
	v_add_f32_e32 v11, v11, v43
	v_add_f32_e32 v12, v12, v44
	v_add_f32_e32 v13, v13, v45
	v_add_f32_e32 v14, v14, v46
	v_add_f32_e32 v15, v15, v47
	v_add_f32_e32 v16, v16, v48
	v_add_f32_e32 v17, v17, v49
	v_add_f32_e32 v18, v18, v50
	v_add_f32_e32 v19, v19, v51
	v_add_f32_e32 v20, v20, v52
	v_add_f32_e32 v21, v21, v53
	v_add_f32_e32 v22, v22, v54
	v_add_f32_e32 v23, v23, v55
	v_add_f32_e32 v24, v24, v56
	v_add_f32_e32 v25, v25, v57
	v_add_f32_e32 v26, v26, v58
	v_add_f32_e32 v27, v27, v59
	v_add_f32_e32 v28, v28, v60
	v_add_f32_e32 v29, v29, v61
	v_add_f32_e32 v30, v30, v62
	v_add_f32_e32 v31, v31, v63
	v_add_f32_e32 v32, v32, v64
	v_add_f32_e32 v33, v33, v65
	v_add_f32_e32 v34, v34, v66
	v_add_f32_e32 v35, v35, v67
	v_add_f32_e32 v36, v36, v68
	v_add_f32_e32 v37, v37, v69
	v_add_f32_e32 v38, v38, v70
	v_add_f32_e32 v39, v39, v71
	s_and_b64 exec, exec, s[6:7]
	v_cvt_pk_f16_f32 v80, v8, v9
	v_cvt_pk_f16_f32 v81, v10, v11
	v_cvt_pk_f16_f32 v82, v12, v13
	v_cvt_pk_f16_f32 v83, v14, v15
	global_store_dwordx4 v1, v[80:83], s[30:31] offset:1088
	s_nop 1
	v_cvt_pk_f16_f32 v80, v16, v17
	v_cvt_pk_f16_f32 v81, v18, v19
	v_cvt_pk_f16_f32 v82, v20, v21
	v_cvt_pk_f16_f32 v83, v22, v23
	global_store_dwordx4 v1, v[80:83], s[30:31] offset:1104
	s_nop 1
	v_cvt_pk_f16_f32 v80, v24, v25
	v_cvt_pk_f16_f32 v81, v26, v27
	v_cvt_pk_f16_f32 v82, v28, v29
	v_cvt_pk_f16_f32 v83, v30, v31
	global_store_dwordx4 v1, v[80:83], s[30:31] offset:1120
	s_nop 1
	v_cvt_pk_f16_f32 v80, v32, v33
	v_cvt_pk_f16_f32 v81, v34, v35
	v_cvt_pk_f16_f32 v82, v36, v37
	v_cvt_pk_f16_f32 v83, v38, v39
	global_store_dwordx4 v1, v[80:83], s[30:31] offset:1136

	.amdhsa_kernel _Z13stage0_kernel5TJobs6S0Args
		.amdhsa_group_segment_fixed_size 26624
		.amdhsa_private_segment_fixed_size 0
		.amdhsa_kernarg_size 568
		.amdhsa_user_sgpr_count 2
		.amdhsa_user_sgpr_dispatch_ptr 0
		.amdhsa_user_sgpr_queue_ptr 0
		.amdhsa_user_sgpr_kernarg_segment_ptr 1
		.amdhsa_user_sgpr_dispatch_id 0
		.amdhsa_user_sgpr_kernarg_preload_length 0
		.amdhsa_user_sgpr_kernarg_preload_offset 0
		.amdhsa_user_sgpr_private_segment_size 0
		.amdhsa_uses_dynamic_stack 0
		.amdhsa_enable_private_segment 0
		.amdhsa_system_sgpr_workgroup_id_x 1
		.amdhsa_system_sgpr_workgroup_id_y 0
		.amdhsa_system_sgpr_workgroup_id_z 0
		.amdhsa_system_sgpr_workgroup_info 0
		.amdhsa_system_vgpr_workitem_id 0
		.amdhsa_next_free_vgpr 96
		.amdhsa_next_free_sgpr 100
		.amdhsa_accum_offset 96
		.amdhsa_reserve_vcc 1
		.amdhsa_float_round_mode_32 0
		.amdhsa_float_round_mode_16_64 0
		.amdhsa_float_denorm_mode_32 3
		.amdhsa_float_denorm_mode_16_64 3
		.amdhsa_dx10_clamp 1
		.amdhsa_ieee_mode 1
		.amdhsa_fp16_overflow 0
		.amdhsa_tg_split 0
		.amdhsa_exception_fp_ieee_invalid_op 0
		.amdhsa_exception_fp_denorm_src 0
		.amdhsa_exception_fp_ieee_div_zero 0
		.amdhsa_exception_fp_ieee_overflow 0
		.amdhsa_exception_fp_ieee_underflow 0
		.amdhsa_exception_fp_ieee_inexact 0
		.amdhsa_exception_int_div_zero 0
	.end_amdhsa_kernel

amdhsa.kernels:
  - .agpr_count:     0
    .args:
      - .offset:         0
        .size:           288
        .value_kind:     by_value
      - .offset:         288
        .size:           280
        .value_kind:     by_value
    .group_segment_fixed_size: 26624
    .kernarg_segment_align: 8
    .kernarg_segment_size: 568
    .language:       OpenCL C
    .language_version:
      - 2
      - 0
    .max_flat_workgroup_size: 256
    .name:           _Z13stage0_kernel5TJobs6S0Args
    .private_segment_fixed_size: 0
    .sgpr_count:     106
    .sgpr_spill_count: 213
    .symbol:         _Z13stage0_kernel5TJobs6S0Args.kd
    .uniform_work_group_size: 1
    .uses_dynamic_stack: false
    .vgpr_count:     96
    .vgpr_spill_count: 0
    .wavefront_size: 64
  - .agpr_count:     0
    .args:
      - .actual_access:  read_only
        .address_space:  global
        .offset:         0
        .size:           8
        .value_kind:     global_buffer
      - .actual_access:  read_only
        .address_space:  global
        .offset:         8
        .size:           8
        .value_kind:     global_buffer
      - .actual_access:  write_only
        .address_space:  global
        .offset:         16
        .size:           8
        .value_kind:     global_buffer
      - .offset:         24
        .size:           4
        .value_kind:     by_value
      - .offset:         28
        .size:           4
        .value_kind:     by_value
    .group_segment_fixed_size: 0
    .kernarg_segment_align: 8
    .kernarg_segment_size: 32
    .language:       OpenCL C
    .language_version:
      - 2
      - 0
    .max_flat_workgroup_size: 256
    .name:           _Z11gelu_reducePKfS0_PDF16_ii
    .private_segment_fixed_size: 0
    .sgpr_count:     18
    .sgpr_spill_count: 0
    .symbol:         _Z11gelu_reducePKfS0_PDF16_ii.kd
    .uniform_work_group_size: 1
    .uses_dynamic_stack: false
    .vgpr_count:     17
    .vgpr_spill_count: 0
    .wavefront_size: 64
  - .agpr_count:     0
    .args:
      - .address_space:  global
        .offset:         0
        .size:           8
        .value_kind:     global_buffer
      - .address_space:  global
        .offset:         8
        .size:           8
        .value_kind:     global_buffer
      - .actual_access:  read_only
        .address_space:  global
        .offset:         16
        .size:           8
        .value_kind:     global_buffer
      - .actual_access:  write_only
        .address_space:  global
        .offset:         24
        .size:           8
        .value_kind:     global_buffer
    .group_segment_fixed_size: 75776
    .kernarg_segment_align: 8
    .kernarg_segment_size: 32
    .language:       OpenCL C
    .language_version:
      - 2
      - 0
    .max_flat_workgroup_size: 512
    .name:           _Z11front_statsPKDF16_S0_PKfPf
    .private_segment_fixed_size: 0
    .sgpr_count:     18
    .sgpr_spill_count: 0
    .symbol:         _Z11front_statsPKDF16_S0_PKfPf.kd
    .uniform_work_group_size: 1
    .uses_dynamic_stack: false
    .vgpr_count:     86
    .vgpr_spill_count: 0
    .wavefront_size: 64
  - .agpr_count:     0
    .args:
      - .actual_access:  read_only
        .address_space:  global
        .offset:         0
        .size:           8
        .value_kind:     global_buffer
      - .actual_access:  read_only
        .address_space:  global
        .offset:         8
        .size:           8
        .value_kind:     global_buffer
      - .actual_access:  read_only
        .address_space:  global
        .offset:         16
        .size:           8
        .value_kind:     global_buffer
      - .actual_access:  read_only
        .address_space:  global
        .offset:         24
        .size:           8
        .value_kind:     global_buffer
      - .actual_access:  read_only
        .address_space:  global
        .offset:         32
        .size:           8
        .value_kind:     global_buffer
      - .actual_access:  read_only
        .address_space:  global
        .offset:         40
        .size:           8
        .value_kind:     global_buffer
      - .actual_access:  read_only
        .address_space:  global
        .offset:         48
        .size:           8
        .value_kind:     global_buffer
      - .actual_access:  write_only
        .address_space:  global
        .offset:         56
        .size:           8
        .value_kind:     global_buffer
    .group_segment_fixed_size: 49152
    .kernarg_segment_align: 8
    .kernarg_segment_size: 64
    .language:       OpenCL C
    .language_version:
      - 2
      - 0
    .max_flat_workgroup_size: 256
    .name:           _Z12attn2_kernelPKDF16_S0_PKfS2_S2_PKiS2_PDF16_
    .private_segment_fixed_size: 0
    .sgpr_count:     82
    .sgpr_spill_count: 0
    .symbol:         _Z12attn2_kernelPKDF16_S0_PKfS2_S2_PKiS2_PDF16_.kd
    .uniform_work_group_size: 1
    .uses_dynamic_stack: false
    .vgpr_count:     166
    .vgpr_spill_count: 0
    .wavefront_size: 64
  - .agpr_count:     0
    .args:
      - .address_space:  global
        .offset:         0
        .size:           8
        .value_kind:     global_buffer
      - .offset:         8
        .size:           4
        .value_kind:     by_value
      - .offset:         12
        .size:           4
        .value_kind:     by_value
      - .address_space:  global
        .offset:         16
        .size:           8
        .value_kind:     global_buffer
      - .offset:         24
        .size:           4
        .value_kind:     by_value
      - .offset:         28
        .size:           4
        .value_kind:     by_value
      - .offset:         32
        .size:           4
        .value_kind:     by_value
      - .offset:         36
        .size:           4
        .value_kind:     by_value
      - .offset:         40
        .size:           4
        .value_kind:     by_value
      - .actual_access:  read_only
        .address_space:  global
        .offset:         48
        .size:           8
        .value_kind:     global_buffer
      - .actual_access:  write_only
        .address_space:  global
        .offset:         56
        .size:           8
        .value_kind:     global_buffer
      - .actual_access:  write_only
        .address_space:  global
        .offset:         64
        .size:           8
        .value_kind:     global_buffer
      - .offset:         72
        .size:           4
        .value_kind:     by_value
    .group_segment_fixed_size: 73728
    .kernarg_segment_align: 8
    .kernarg_segment_size: 76
    .language:       OpenCL C
    .language_version:
      - 2
      - 0
    .max_flat_workgroup_size: 512
    .name:           _Z11gemm_kernelILi2ELi4ELi2ELi2ELi3ELi0ELi4ELb0EEvPKDF16_iiS1_iiiiiPKfPfPDF16_i
    .private_segment_fixed_size: 0
    .sgpr_count:     33
    .sgpr_spill_count: 0
    .symbol:         _Z11gemm_kernelILi2ELi4ELi2ELi2ELi3ELi0ELi4ELb0EEvPKDF16_iiS1_iiiiiPKfPfPDF16_i.kd
    .uniform_work_group_size: 1
    .uses_dynamic_stack: false
    .vgpr_count:     96
    .vgpr_spill_count: 0
    .wavefront_size: 64
  - .agpr_count:     0
    .args:
      - .address_space:  global
        .offset:         0
        .size:           8
        .value_kind:     global_buffer
      - .offset:         8
        .size:           4
        .value_kind:     by_value
      - .offset:         12
        .size:           4
        .value_kind:     by_value
      - .address_space:  global
        .offset:         16
        .size:           8
        .value_kind:     global_buffer
      - .offset:         24
        .size:           4
        .value_kind:     by_value
      - .offset:         28
        .size:           4
        .value_kind:     by_value
      - .offset:         32
        .size:           4
        .value_kind:     by_value
      - .offset:         36
        .size:           4
        .value_kind:     by_value
      - .offset:         40
        .size:           4
        .value_kind:     by_value
      - .actual_access:  read_only
        .address_space:  global
        .offset:         48
        .size:           8
        .value_kind:     global_buffer
      - .actual_access:  write_only
        .address_space:  global
        .offset:         56
        .size:           8
        .value_kind:     global_buffer
      - .actual_access:  read_only
        .address_space:  global
        .offset:         64
        .size:           8
        .value_kind:     global_buffer
      - .offset:         72
        .size:           4
        .value_kind:     by_value
    .group_segment_fixed_size: 163840
    .kernarg_segment_align: 8
    .kernarg_segment_size: 76
    .language:       OpenCL C
    .language_version:
      - 2
      - 0
    .max_flat_workgroup_size: 512
    .name:           _Z11gemm_kernelILi4ELi2ELi2ELi4ELi4ELi3ELi2ELb0EEvPKDF16_iiS1_iiiiiPKfPfPDF16_i
    .private_segment_fixed_size: 0
    .sgpr_count:     35
    .sgpr_spill_count: 0
    .symbol:         _Z11gemm_kernelILi4ELi2ELi2ELi4ELi4ELi3ELi2ELb0EEvPKDF16_iiS1_iiiiiPKfPfPDF16_i.kd
    .uniform_work_group_size: 1
    .uses_dynamic_stack: false
    .vgpr_count:     200
    .vgpr_spill_count: 0
    .wavefront_size: 64
  - .agpr_count:     0
    .args:
      - .address_space:  global
        .offset:         0
        .size:           8
        .value_kind:     global_buffer
      - .offset:         8
        .size:           4
        .value_kind:     by_value
      - .offset:         12
        .size:           4
        .value_kind:     by_value
      - .address_space:  global
        .offset:         16
        .size:           8
        .value_kind:     global_buffer
      - .offset:         24
        .size:           4
        .value_kind:     by_value
      - .offset:         28
        .size:           4
        .value_kind:     by_value
      - .offset:         32
        .size:           4
        .value_kind:     by_value
      - .offset:         36
        .size:           4
        .value_kind:     by_value
      - .offset:         40
        .size:           4
        .value_kind:     by_value
      - .actual_access:  read_only
        .address_space:  global
        .offset:         48
        .size:           8
        .value_kind:     global_buffer
      - .actual_access:  write_only
        .address_space:  global
        .offset:         56
        .size:           8
        .value_kind:     global_buffer
      - .actual_access:  read_only
        .address_space:  global
        .offset:         64
        .size:           8
        .value_kind:     global_buffer
      - .offset:         72
        .size:           4
        .value_kind:     by_value
    .group_segment_fixed_size: 65536
    .kernarg_segment_align: 8
    .kernarg_segment_size: 76
    .language:       OpenCL C
    .language_version:
      - 2
      - 0
    .max_flat_workgroup_size: 512
    .name:           _Z11gemm_kernelILi2ELi4ELi2ELi1ELi4ELi2ELi2ELb0EEvPKDF16_iiS1_iiiiiPKfPfPDF16_i
    .private_segment_fixed_size: 0
    .sgpr_count:     26
    .sgpr_spill_count: 0
    .symbol:         _Z11gemm_kernelILi2ELi4ELi2ELi1ELi4ELi2ELi2ELb0EEvPKDF16_iiS1_iiiiiPKfPfPDF16_i.kd
    .uniform_work_group_size: 1
    .uses_dynamic_stack: false
    .vgpr_count:     64
    .vgpr_spill_count: 0
    .wavefront_size: 64
